# v57 + back-edge rotation of the five fp8 GEMM K-loops: counter update and exit compare ahead of the loop-back barrier, steady trips branch from the barrier straight to the first load segment
# speedup vs baseline: 1.0031x; 1.0031x over previous
.Lp1_fast:
.Lp1_join:
	ds_read_b128 v[136:139], v246 offset:0
	ds_read_b128 v[144:147], v246 offset:2048
	ds_read_b128 v[140:143], v247 offset:0
	ds_read_b128 v[148:151], v247 offset:2048
	ds_read_b128 v[152:155], v246 offset:16384
	ds_read_b128 v[160:163], v246 offset:18432
	ds_read_b128 v[156:159], v247 offset:16384
	ds_read_b128 v[164:167], v247 offset:18432
	s_add_i32 s10, s97, 0xffffff80
	s_add_i32 s11, s10, s94
	s_cmpk_eq_i32 s97, 0x880
	s_cselect_b32 s40, s37, s91
	s_cselect_b32 s10, 0, s10
	s_cselect_b32 s39, 0x80, s97
	s_cselect_b32 s38, s36, s11
	s_add_i32 s11, s91, s97
	s_add_i32 s39, s40, s39
	s_addk_i32 s11, 0xff00
	s_add_i32 s40, s40, s10
	s_mov_b32 m0, s72
	ds_read_b128 v[168:171], v252
	ds_read_b128 v[176:179], v252 offset:2048
	ds_read_b128 v[172:175], v253
	ds_read_b128 v[180:183], v253 offset:2048
	ds_read_b128 v[184:187], v252 offset:4096
	ds_read_b128 v[192:195], v252 offset:6144
	ds_read_b128 v[188:191], v253 offset:4096
	ds_read_b128 v[196:199], v253 offset:6144
	buffer_load_dwordx4 v250, s[12:15], s11 offen lds
	s_mov_b32 m0, s75
	s_nop 0
	buffer_load_dwordx4 v251, s[12:15], s11 offen lds
	s_waitcnt vmcnt(8)
	s_waitcnt lgkmcnt(0)
	s_barrier
	s_setprio 1
	s_waitcnt lgkmcnt(5)
	v_mfma_f32_16x16x128_f8f6f4 v[124:127], v[136:143], v[168:175], v[124:127]
	v_mfma_f32_16x16x128_f8f6f4 v[120:123], v[144:151], v[168:175], v[120:123]
	s_waitcnt lgkmcnt(4)
	v_mfma_f32_16x16x128_f8f6f4 v[112:115], v[136:143], v[176:183], v[112:115]
	v_mfma_f32_16x16x128_f8f6f4 v[104:107], v[144:151], v[176:183], v[104:107]
	s_waitcnt lgkmcnt(1)
	v_mfma_f32_16x16x128_f8f6f4 v[96:99], v[136:143], v[184:191], v[96:99]
	v_mfma_f32_16x16x128_f8f6f4 v[128:131], v[144:151], v[184:191], v[88:91]
	s_waitcnt lgkmcnt(0)
	v_mfma_f32_16x16x128_f8f6f4 v[200:203], v[136:143], v[192:199], v[80:83]
	v_mfma_f32_16x16x128_f8f6f4 v[204:207], v[144:151], v[192:199], v[72:75]
	s_setprio 0
	s_setprio 1
	v_mfma_f32_16x16x128_f8f6f4 v[116:119], v[152:159], v[168:175], v[116:119]
	v_mfma_f32_16x16x128_f8f6f4 v[108:111], v[160:167], v[168:175], v[108:111]
	v_mfma_f32_16x16x128_f8f6f4 v[100:103], v[152:159], v[176:183], v[100:103]
	v_mfma_f32_16x16x128_f8f6f4 v[168:171], v[160:167], v[176:183], v[92:95]
	v_mfma_f32_16x16x128_f8f6f4 v[172:175], v[152:159], v[184:191], v[84:87]
	v_mfma_f32_16x16x128_f8f6f4 v[176:179], v[160:167], v[184:191], v[76:79]
	v_mfma_f32_16x16x128_f8f6f4 v[180:183], v[152:159], v[192:199], v[68:71]
	v_mfma_f32_16x16x128_f8f6f4 v[184:187], v[160:167], v[192:199], v[64:67]
	s_setprio 0
	s_barrier
	s_mov_b32 m0, s57
	s_mov_b32 s10, s14
	s_mov_b32 s11, s15
	s_nop 1
	ds_read_b128 v[64:67], v252 offset:16384
	ds_read_b128 v[72:75], v252 offset:18432
	ds_read_b128 v[68:71], v253 offset:16384
	ds_read_b128 v[76:79], v253 offset:18432
	ds_read_b128 v[80:83], v252 offset:20480
	ds_read_b128 v[88:91], v252 offset:22528
	ds_read_b128 v[84:87], v253 offset:20480
	ds_read_b128 v[92:95], v253 offset:22528
	buffer_load_dwordx4 v244, s[8:11], s38 offen lds
	s_mov_b32 m0, s58
	s_add_i32 s41, s38, 0x40000
	buffer_load_dwordx4 v245, s[8:11], s38 offen lds
	s_mov_b32 m0, s59
	s_nop 0
	buffer_load_dwordx4 v244, s[8:11], s41 offen lds
	s_mov_b32 m0, s60
	s_nop 0
	buffer_load_dwordx4 v245, s[8:11], s41 offen lds
	s_mov_b32 m0, s56
	s_nop 0
	buffer_load_dwordx4 v248, s[12:15], s40 offen lds
	s_mov_b32 m0, s61
	s_nop 0
	buffer_load_dwordx4 v249, s[12:15], s40 offen lds
	s_waitcnt vmcnt(8)
	s_waitcnt lgkmcnt(0)
	s_barrier
	s_setprio 1
	s_waitcnt lgkmcnt(5)
	v_mfma_f32_16x16x128_f8f6f4 v[60:63], v[136:143], v[64:71], v[60:63]
	v_mfma_f32_16x16x128_f8f6f4 v[56:59], v[144:151], v[64:71], v[56:59]
	s_waitcnt lgkmcnt(4)
	v_mfma_f32_16x16x128_f8f6f4 v[48:51], v[136:143], v[72:79], v[48:51]
	v_mfma_f32_16x16x128_f8f6f4 v[188:191], v[144:151], v[72:79], v[40:43]
	s_waitcnt lgkmcnt(1)
	v_mfma_f32_16x16x128_f8f6f4 v[192:195], v[136:143], v[80:87], v[32:35]
	v_mfma_f32_16x16x128_f8f6f4 v[196:199], v[144:151], v[80:87], v[24:27]
	s_waitcnt lgkmcnt(0)
	v_mfma_f32_16x16x128_f8f6f4 v[208:211], v[136:143], v[88:95], v[16:19]
	v_mfma_f32_16x16x128_f8f6f4 v[212:215], v[144:151], v[88:95], v[8:11]
	s_setprio 0
	s_setprio 1
	v_mfma_f32_16x16x128_f8f6f4 v[52:55], v[152:159], v[64:71], v[52:55]
	v_mfma_f32_16x16x128_f8f6f4 v[216:219], v[160:167], v[64:71], v[44:47]
	v_mfma_f32_16x16x128_f8f6f4 v[220:223], v[152:159], v[72:79], v[36:39]
	v_mfma_f32_16x16x128_f8f6f4 v[224:227], v[160:167], v[72:79], v[28:31]
	v_mfma_f32_16x16x128_f8f6f4 v[228:231], v[152:159], v[80:87], v[20:23]
	v_mfma_f32_16x16x128_f8f6f4 v[232:235], v[160:167], v[80:87], v[12:15]
	v_mfma_f32_16x16x128_f8f6f4 v[236:239], v[152:159], v[88:95], v[4:7]
	v_mfma_f32_16x16x128_f8f6f4 v[240:243], v[160:167], v[88:95], v[0:3]
	s_setprio 0
	s_barrier
	s_add_i32 s41, 0, 0x18000
	s_nop 2
	s_add_i32 s41, 0, 0x1c000
	ds_read_b128 v[0:3], v246 offset:32768
	ds_read_b128 v[8:11], v246 offset:34816
	ds_read_b128 v[4:7], v247 offset:32768
	ds_read_b128 v[12:15], v247 offset:34816
	ds_read_b128 v[136:139], v246 offset:49152
	ds_read_b128 v[144:147], v246 offset:51200
	ds_read_b128 v[140:143], v247 offset:49152
	ds_read_b128 v[148:151], v247 offset:51200
	s_mov_b32 m0, s62
	ds_read_b128 v[16:19], v252 offset:32768
	ds_read_b128 v[24:27], v252 offset:34816
	ds_read_b128 v[20:23], v253 offset:32768
	ds_read_b128 v[28:31], v253 offset:34816
	ds_read_b128 v[32:35], v252 offset:36864
	ds_read_b128 v[40:43], v252 offset:38912
	ds_read_b128 v[36:39], v253 offset:36864
	ds_read_b128 v[44:47], v253 offset:38912
	buffer_load_dwordx4 v250, s[12:15], s40 offen lds
	s_mov_b32 m0, s63
	s_nop 0
	buffer_load_dwordx4 v251, s[12:15], s40 offen lds
	s_waitcnt vmcnt(8)
	s_waitcnt lgkmcnt(0)
	s_barrier
	s_setprio 1
	s_waitcnt lgkmcnt(5)
	v_mfma_f32_16x16x128_f8f6f4 v[124:127], v[0:7], v[16:23], v[124:127]
	v_mfma_f32_16x16x128_f8f6f4 v[120:123], v[8:15], v[16:23], v[120:123]
	s_waitcnt lgkmcnt(4)
	v_mfma_f32_16x16x128_f8f6f4 v[112:115], v[0:7], v[24:31], v[112:115]
	v_mfma_f32_16x16x128_f8f6f4 v[104:107], v[8:15], v[24:31], v[104:107]
	s_waitcnt lgkmcnt(1)
	v_mfma_f32_16x16x128_f8f6f4 v[96:99], v[0:7], v[32:39], v[96:99]
	v_mfma_f32_16x16x128_f8f6f4 v[88:91], v[8:15], v[32:39], v[128:131]
	s_waitcnt lgkmcnt(0)
	v_mfma_f32_16x16x128_f8f6f4 v[80:83], v[0:7], v[40:47], v[200:203]
	v_mfma_f32_16x16x128_f8f6f4 v[72:75], v[8:15], v[40:47], v[204:207]
	s_setprio 0
	s_setprio 1
	v_mfma_f32_16x16x128_f8f6f4 v[116:119], v[136:143], v[16:23], v[116:119]
	v_mfma_f32_16x16x128_f8f6f4 v[108:111], v[144:151], v[16:23], v[108:111]
	v_mfma_f32_16x16x128_f8f6f4 v[100:103], v[136:143], v[24:31], v[100:103]
	v_mfma_f32_16x16x128_f8f6f4 v[92:95], v[144:151], v[24:31], v[168:171]
	v_mfma_f32_16x16x128_f8f6f4 v[84:87], v[136:143], v[32:39], v[172:175]
	v_mfma_f32_16x16x128_f8f6f4 v[76:79], v[144:151], v[32:39], v[176:179]
	v_mfma_f32_16x16x128_f8f6f4 v[68:71], v[136:143], v[40:47], v[180:183]
	v_mfma_f32_16x16x128_f8f6f4 v[64:67], v[144:151], v[40:47], v[184:187]
	s_setprio 0
	s_barrier
	s_mov_b32 m0, s64
	s_add_i32 s40, s38, 0x80
	ds_read_b128 v[152:155], v252 offset:49152
	ds_read_b128 v[160:163], v252 offset:51200
	ds_read_b128 v[156:159], v253 offset:49152
	ds_read_b128 v[164:167], v253 offset:51200
	ds_read_b128 v[168:171], v252 offset:53248
	ds_read_b128 v[176:179], v252 offset:55296
	ds_read_b128 v[172:175], v253 offset:53248
	ds_read_b128 v[180:183], v253 offset:55296
	buffer_load_dwordx4 v244, s[8:11], s40 offen lds
	s_mov_b32 m0, s65
	s_add_i32 s38, s38, 0x40080
	buffer_load_dwordx4 v245, s[8:11], s40 offen lds
	s_mov_b32 m0, s68
	s_nop 0
	buffer_load_dwordx4 v244, s[8:11], s38 offen lds
	s_mov_b32 m0, s69
	s_nop 0
	buffer_load_dwordx4 v245, s[8:11], s38 offen lds
	s_mov_b32 m0, s66
	s_nop 0
	buffer_load_dwordx4 v248, s[12:15], s39 offen lds
	s_mov_b32 m0, s67
	s_nop 0
	buffer_load_dwordx4 v249, s[12:15], s39 offen lds
	s_waitcnt vmcnt(8)
	s_waitcnt lgkmcnt(0)
	s_barrier
	s_setprio 1
	s_waitcnt lgkmcnt(5)
	v_mfma_f32_16x16x128_f8f6f4 v[60:63], v[0:7], v[152:159], v[60:63]
	v_mfma_f32_16x16x128_f8f6f4 v[56:59], v[8:15], v[152:159], v[56:59]
	s_waitcnt lgkmcnt(4)
	v_mfma_f32_16x16x128_f8f6f4 v[48:51], v[0:7], v[160:167], v[48:51]
	v_mfma_f32_16x16x128_f8f6f4 v[40:43], v[8:15], v[160:167], v[188:191]
	s_waitcnt lgkmcnt(1)
	v_mfma_f32_16x16x128_f8f6f4 v[32:35], v[0:7], v[168:175], v[192:195]
	v_mfma_f32_16x16x128_f8f6f4 v[24:27], v[8:15], v[168:175], v[196:199]
	s_waitcnt lgkmcnt(0)
	v_mfma_f32_16x16x128_f8f6f4 v[16:19], v[0:7], v[176:183], v[208:211]
	v_mfma_f32_16x16x128_f8f6f4 v[8:11], v[8:15], v[176:183], v[212:215]
	s_setprio 0
	s_setprio 1
	v_mfma_f32_16x16x128_f8f6f4 v[52:55], v[136:143], v[152:159], v[52:55]
	v_mfma_f32_16x16x128_f8f6f4 v[44:47], v[144:151], v[152:159], v[216:219]
	v_mfma_f32_16x16x128_f8f6f4 v[36:39], v[136:143], v[160:167], v[220:223]
	v_mfma_f32_16x16x128_f8f6f4 v[28:31], v[144:151], v[160:167], v[224:227]
	v_mfma_f32_16x16x128_f8f6f4 v[20:23], v[136:143], v[168:175], v[228:231]
	v_mfma_f32_16x16x128_f8f6f4 v[12:15], v[144:151], v[168:175], v[232:235]
	v_mfma_f32_16x16x128_f8f6f4 v[4:7], v[136:143], v[176:183], v[236:239]
	v_mfma_f32_16x16x128_f8f6f4 v[0:3], v[144:151], v[176:183], v[240:243]
	s_setprio 0
	s_add_i32 s96, s96, 2
	s_addk_i32 s97, 0x100
	s_cmp_gt_u32 s96, 13
	s_barrier
	s_cbranch_scc1 .LBB0_1022
	s_cmpk_lg_i32 s97, 0x780
	s_cbranch_scc1 .Lp1_join

.Lp5_fast:
.Lp5_join:
	ds_read_b128 v[136:139], v244 offset:0
	ds_read_b128 v[144:147], v244 offset:2048
	ds_read_b128 v[140:143], v245 offset:0
	ds_read_b128 v[148:151], v245 offset:2048
	ds_read_b128 v[152:155], v244 offset:16384
	ds_read_b128 v[160:163], v244 offset:18432
	ds_read_b128 v[156:159], v245 offset:16384
	ds_read_b128 v[164:167], v245 offset:18432
	s_add_i32 s6, s62, 0xffffff80
	s_add_i32 s7, s6, s57
	s_cmpk_eq_i32 s62, 0x880
	s_cselect_b32 s65, s35, s54
	s_cselect_b32 s6, 0, s6
	s_cselect_b32 s64, 0x80, s62
	s_cselect_b32 s63, s29, s7
	s_add_i32 s7, s54, s62
	s_add_i32 s64, s65, s64
	s_addk_i32 s7, 0xff00
	s_add_i32 s65, s65, s6
	s_mov_b32 m0, s44
	ds_read_b128 v[168:171], v250
	ds_read_b128 v[176:179], v250 offset:2048
	ds_read_b128 v[172:175], v251
	ds_read_b128 v[180:183], v251 offset:2048
	ds_read_b128 v[184:187], v250 offset:4096
	ds_read_b128 v[192:195], v250 offset:6144
	ds_read_b128 v[188:191], v251 offset:4096
	ds_read_b128 v[196:199], v251 offset:6144
	buffer_load_dwordx4 v248, s[8:11], s7 offen lds
	s_mov_b32 m0, s47
	s_nop 0
	buffer_load_dwordx4 v249, s[8:11], s7 offen lds
	s_waitcnt vmcnt(8)
	s_waitcnt lgkmcnt(0)
	s_barrier
	s_setprio 1
	s_waitcnt lgkmcnt(5)
	v_mfma_f32_16x16x128_f8f6f4 v[124:127], v[136:143], v[168:175], v[124:127]
	v_mfma_f32_16x16x128_f8f6f4 v[120:123], v[144:151], v[168:175], v[120:123]
	s_waitcnt lgkmcnt(4)
	v_mfma_f32_16x16x128_f8f6f4 v[108:111], v[136:143], v[176:183], v[108:111]
	v_mfma_f32_16x16x128_f8f6f4 v[104:107], v[144:151], v[176:183], v[104:107]
	s_waitcnt lgkmcnt(1)
	v_mfma_f32_16x16x128_f8f6f4 v[128:131], v[136:143], v[184:191], v[92:95]
	v_mfma_f32_16x16x128_f8f6f4 v[200:203], v[144:151], v[184:191], v[88:91]
	s_waitcnt lgkmcnt(0)
	v_mfma_f32_16x16x128_f8f6f4 v[204:207], v[136:143], v[192:199], v[76:79]
	v_mfma_f32_16x16x128_f8f6f4 v[208:211], v[144:151], v[192:199], v[72:75]
	s_setprio 0
	s_setprio 1
	v_mfma_f32_16x16x128_f8f6f4 v[116:119], v[152:159], v[168:175], v[116:119]
	v_mfma_f32_16x16x128_f8f6f4 v[112:115], v[160:167], v[168:175], v[112:115]
	v_mfma_f32_16x16x128_f8f6f4 v[100:103], v[152:159], v[176:183], v[100:103]
	v_mfma_f32_16x16x128_f8f6f4 v[96:99], v[160:167], v[176:183], v[96:99]
	v_mfma_f32_16x16x128_f8f6f4 v[168:171], v[152:159], v[184:191], v[84:87]
	v_mfma_f32_16x16x128_f8f6f4 v[172:175], v[160:167], v[184:191], v[80:83]
	v_mfma_f32_16x16x128_f8f6f4 v[176:179], v[152:159], v[192:199], v[68:71]
	v_mfma_f32_16x16x128_f8f6f4 v[180:183], v[160:167], v[192:199], v[64:67]
	s_setprio 0
	s_barrier
	s_mov_b32 m0, s26
	s_mov_b32 s6, s10
	s_mov_b32 s7, s11
	s_nop 1
	ds_read_b128 v[64:67], v250 offset:16384
	ds_read_b128 v[72:75], v250 offset:18432
	ds_read_b128 v[68:71], v251 offset:16384
	ds_read_b128 v[76:79], v251 offset:18432
	ds_read_b128 v[80:83], v250 offset:20480
	ds_read_b128 v[88:91], v250 offset:22528
	ds_read_b128 v[84:87], v251 offset:20480
	ds_read_b128 v[92:95], v251 offset:22528
	buffer_load_dwordx4 v132, s[4:7], s63 offen lds
	s_mov_b32 m0, s27
	s_add_i32 s66, s63, 0x40000
	buffer_load_dwordx4 v133, s[4:7], s63 offen lds
	s_mov_b32 m0, s28
	s_nop 0
	buffer_load_dwordx4 v132, s[4:7], s66 offen lds
	s_mov_b32 m0, s30
	s_nop 0
	buffer_load_dwordx4 v133, s[4:7], s66 offen lds
	s_mov_b32 m0, s25
	s_nop 0
	buffer_load_dwordx4 v246, s[8:11], s65 offen lds
	s_mov_b32 m0, s31
	s_nop 0
	buffer_load_dwordx4 v247, s[8:11], s65 offen lds
	s_waitcnt vmcnt(8)
	s_waitcnt lgkmcnt(0)
	s_barrier
	s_setprio 1
	s_waitcnt lgkmcnt(5)
	v_mfma_f32_16x16x128_f8f6f4 v[60:63], v[136:143], v[64:71], v[60:63]
	v_mfma_f32_16x16x128_f8f6f4 v[56:59], v[144:151], v[64:71], v[56:59]
	s_waitcnt lgkmcnt(4)
	v_mfma_f32_16x16x128_f8f6f4 v[184:187], v[136:143], v[72:79], v[44:47]
	v_mfma_f32_16x16x128_f8f6f4 v[188:191], v[144:151], v[72:79], v[40:43]
	s_waitcnt lgkmcnt(1)
	v_mfma_f32_16x16x128_f8f6f4 v[192:195], v[136:143], v[80:87], v[28:31]
	v_mfma_f32_16x16x128_f8f6f4 v[196:199], v[144:151], v[80:87], v[24:27]
	s_waitcnt lgkmcnt(0)
	v_mfma_f32_16x16x128_f8f6f4 v[212:215], v[136:143], v[88:95], v[12:15]
	v_mfma_f32_16x16x128_f8f6f4 v[216:219], v[144:151], v[88:95], v[8:11]
	s_setprio 0
	s_setprio 1
	v_mfma_f32_16x16x128_f8f6f4 v[52:55], v[152:159], v[64:71], v[52:55]
	v_mfma_f32_16x16x128_f8f6f4 v[48:51], v[160:167], v[64:71], v[48:51]
	v_mfma_f32_16x16x128_f8f6f4 v[220:223], v[152:159], v[72:79], v[36:39]
	v_mfma_f32_16x16x128_f8f6f4 v[224:227], v[160:167], v[72:79], v[32:35]
	v_mfma_f32_16x16x128_f8f6f4 v[228:231], v[152:159], v[80:87], v[20:23]
	v_mfma_f32_16x16x128_f8f6f4 v[232:235], v[160:167], v[80:87], v[16:19]
	v_mfma_f32_16x16x128_f8f6f4 v[236:239], v[152:159], v[88:95], v[4:7]
	v_mfma_f32_16x16x128_f8f6f4 v[240:243], v[160:167], v[88:95], v[0:3]
	s_setprio 0
	s_barrier
	s_add_i32 s66, 0, 0x18000
	s_nop 2
	s_add_i32 s66, 0, 0x1c000
	ds_read_b128 v[0:3], v244 offset:32768
	ds_read_b128 v[16:19], v244 offset:34816
	ds_read_b128 v[4:7], v245 offset:32768
	ds_read_b128 v[20:23], v245 offset:34816
	ds_read_b128 v[136:139], v244 offset:49152
	ds_read_b128 v[144:147], v244 offset:51200
	ds_read_b128 v[140:143], v245 offset:49152
	ds_read_b128 v[148:151], v245 offset:51200
	s_mov_b32 m0, s33
	ds_read_b128 v[8:11], v250 offset:32768
	ds_read_b128 v[24:27], v250 offset:34816
	ds_read_b128 v[12:15], v251 offset:32768
	ds_read_b128 v[28:31], v251 offset:34816
	ds_read_b128 v[32:35], v250 offset:36864
	ds_read_b128 v[40:43], v250 offset:38912
	ds_read_b128 v[36:39], v251 offset:36864
	ds_read_b128 v[44:47], v251 offset:38912
	buffer_load_dwordx4 v248, s[8:11], s65 offen lds
	s_mov_b32 m0, s34
	s_nop 0
	buffer_load_dwordx4 v249, s[8:11], s65 offen lds
	s_waitcnt vmcnt(8)
	s_waitcnt lgkmcnt(0)
	s_barrier
	s_setprio 1
	s_waitcnt lgkmcnt(5)
	v_mfma_f32_16x16x128_f8f6f4 v[124:127], v[0:7], v[8:15], v[124:127]
	v_mfma_f32_16x16x128_f8f6f4 v[120:123], v[16:23], v[8:15], v[120:123]
	s_waitcnt lgkmcnt(4)
	v_mfma_f32_16x16x128_f8f6f4 v[108:111], v[0:7], v[24:31], v[108:111]
	v_mfma_f32_16x16x128_f8f6f4 v[104:107], v[16:23], v[24:31], v[104:107]
	s_waitcnt lgkmcnt(1)
	v_mfma_f32_16x16x128_f8f6f4 v[92:95], v[0:7], v[32:39], v[128:131]
	v_mfma_f32_16x16x128_f8f6f4 v[88:91], v[16:23], v[32:39], v[200:203]
	s_waitcnt lgkmcnt(0)
	v_mfma_f32_16x16x128_f8f6f4 v[76:79], v[0:7], v[40:47], v[204:207]
	v_mfma_f32_16x16x128_f8f6f4 v[72:75], v[16:23], v[40:47], v[208:211]
	s_setprio 0
	s_setprio 1
	v_mfma_f32_16x16x128_f8f6f4 v[116:119], v[136:143], v[8:15], v[116:119]
	v_mfma_f32_16x16x128_f8f6f4 v[112:115], v[144:151], v[8:15], v[112:115]
	v_mfma_f32_16x16x128_f8f6f4 v[100:103], v[136:143], v[24:31], v[100:103]
	v_mfma_f32_16x16x128_f8f6f4 v[96:99], v[144:151], v[24:31], v[96:99]
	v_mfma_f32_16x16x128_f8f6f4 v[84:87], v[136:143], v[32:39], v[168:171]
	v_mfma_f32_16x16x128_f8f6f4 v[80:83], v[144:151], v[32:39], v[172:175]
	v_mfma_f32_16x16x128_f8f6f4 v[68:71], v[136:143], v[40:47], v[176:179]
	v_mfma_f32_16x16x128_f8f6f4 v[64:67], v[144:151], v[40:47], v[180:183]
	s_setprio 0
	s_barrier
	s_mov_b32 m0, s36
	s_add_i32 s65, s63, 0x80
	ds_read_b128 v[32:35], v250 offset:49152
	ds_read_b128 v[152:155], v250 offset:51200
	ds_read_b128 v[36:39], v251 offset:49152
	ds_read_b128 v[156:159], v251 offset:51200
	ds_read_b128 v[160:163], v250 offset:53248
	ds_read_b128 v[168:171], v250 offset:55296
	ds_read_b128 v[164:167], v251 offset:53248
	ds_read_b128 v[172:175], v251 offset:55296
	buffer_load_dwordx4 v132, s[4:7], s65 offen lds
	s_mov_b32 m0, s37
	s_add_i32 s63, s63, 0x40080
	buffer_load_dwordx4 v133, s[4:7], s65 offen lds
	s_mov_b32 m0, s40
	s_nop 0
	buffer_load_dwordx4 v132, s[4:7], s63 offen lds
	s_mov_b32 m0, s41
	s_nop 0
	buffer_load_dwordx4 v133, s[4:7], s63 offen lds
	s_mov_b32 m0, s38
	s_nop 0
	buffer_load_dwordx4 v246, s[8:11], s64 offen lds
	s_mov_b32 m0, s39
	s_nop 0
	buffer_load_dwordx4 v247, s[8:11], s64 offen lds
	s_waitcnt vmcnt(8)
	s_waitcnt lgkmcnt(0)
	s_barrier
	s_setprio 1
	s_waitcnt lgkmcnt(5)
	v_mfma_f32_16x16x128_f8f6f4 v[60:63], v[0:7], v[32:39], v[60:63]
	v_mfma_f32_16x16x128_f8f6f4 v[56:59], v[16:23], v[32:39], v[56:59]
	s_waitcnt lgkmcnt(4)
	v_mfma_f32_16x16x128_f8f6f4 v[44:47], v[0:7], v[152:159], v[184:187]
	v_mfma_f32_16x16x128_f8f6f4 v[40:43], v[16:23], v[152:159], v[188:191]
	s_waitcnt lgkmcnt(1)
	v_mfma_f32_16x16x128_f8f6f4 v[28:31], v[0:7], v[160:167], v[192:195]
	v_mfma_f32_16x16x128_f8f6f4 v[24:27], v[16:23], v[160:167], v[196:199]
	s_waitcnt lgkmcnt(0)
	v_mfma_f32_16x16x128_f8f6f4 v[12:15], v[0:7], v[168:175], v[212:215]
	v_mfma_f32_16x16x128_f8f6f4 v[8:11], v[16:23], v[168:175], v[216:219]
	s_setprio 0
	s_setprio 1
	v_mfma_f32_16x16x128_f8f6f4 v[52:55], v[136:143], v[32:39], v[52:55]
	v_mfma_f32_16x16x128_f8f6f4 v[48:51], v[144:151], v[32:39], v[48:51]
	v_mfma_f32_16x16x128_f8f6f4 v[36:39], v[136:143], v[152:159], v[220:223]
	v_mfma_f32_16x16x128_f8f6f4 v[32:35], v[144:151], v[152:159], v[224:227]
	v_mfma_f32_16x16x128_f8f6f4 v[20:23], v[136:143], v[160:167], v[228:231]
	v_mfma_f32_16x16x128_f8f6f4 v[16:19], v[144:151], v[160:167], v[232:235]
	v_mfma_f32_16x16x128_f8f6f4 v[4:7], v[136:143], v[168:175], v[236:239]
	v_mfma_f32_16x16x128_f8f6f4 v[0:3], v[144:151], v[168:175], v[240:243]
	s_setprio 0
	s_add_i32 s61, s61, 2
	s_addk_i32 s62, 0x100
	s_cmp_gt_u32 s61, 13
	s_barrier
	s_cbranch_scc1 .LBB0_2177
	s_cmpk_lg_i32 s62, 0x780
	s_cbranch_scc1 .Lp5_join

.Lp6_fast:
.Lp6_join:
	ds_read_b128 v[128:131], v245 offset:0
	ds_read_b128 v[136:139], v245 offset:2048
	ds_read_b128 v[132:135], v246 offset:0
	ds_read_b128 v[140:143], v246 offset:2048
	ds_read_b128 v[144:147], v245 offset:16384
	ds_read_b128 v[160:163], v245 offset:18432
	ds_read_b128 v[148:151], v246 offset:16384
	ds_read_b128 v[164:167], v246 offset:18432
	s_add_i32 s6, s64, 0xffffff80
	s_add_i32 s7, s6, s59
	s_cmpk_eq_i32 s64, 0x880
	s_cselect_b32 s67, s37, s56
	s_cselect_b32 s6, 0, s6
	s_cselect_b32 s66, 0x80, s64
	s_cselect_b32 s65, s31, s7
	s_add_i32 s7, s56, s64
	s_add_i32 s66, s67, s66
	s_addk_i32 s7, 0xff00
	s_add_i32 s67, s67, s6
	s_mov_b32 m0, s46
	ds_read_b128 v[168:171], v251
	ds_read_b128 v[176:179], v251 offset:2048
	ds_read_b128 v[172:175], v252
	ds_read_b128 v[180:183], v252 offset:2048
	ds_read_b128 v[184:187], v251 offset:4096
	ds_read_b128 v[192:195], v251 offset:6144
	ds_read_b128 v[188:191], v252 offset:4096
	ds_read_b128 v[196:199], v252 offset:6144
	buffer_load_dwordx4 v249, s[8:11], s7 offen lds
	s_mov_b32 m0, s49
	s_nop 0
	buffer_load_dwordx4 v250, s[8:11], s7 offen lds
	s_waitcnt vmcnt(8)
	s_waitcnt lgkmcnt(0)
	s_barrier
	s_setprio 1
	s_waitcnt lgkmcnt(5)
	v_mfma_f32_16x16x128_f8f6f4 v[124:127], v[128:135], v[168:175], v[124:127]
	v_mfma_f32_16x16x128_f8f6f4 v[120:123], v[136:143], v[168:175], v[120:123]
	s_waitcnt lgkmcnt(4)
	v_mfma_f32_16x16x128_f8f6f4 v[108:111], v[128:135], v[176:183], v[108:111]
	v_mfma_f32_16x16x128_f8f6f4 v[104:107], v[136:143], v[176:183], v[104:107]
	s_waitcnt lgkmcnt(1)
	v_mfma_f32_16x16x128_f8f6f4 v[152:155], v[128:135], v[184:191], v[92:95]
	v_mfma_f32_16x16x128_f8f6f4 v[200:203], v[136:143], v[184:191], v[88:91]
	s_waitcnt lgkmcnt(0)
	v_mfma_f32_16x16x128_f8f6f4 v[204:207], v[128:135], v[192:199], v[76:79]
	v_mfma_f32_16x16x128_f8f6f4 v[208:211], v[136:143], v[192:199], v[72:75]
	s_setprio 0
	s_setprio 1
	v_mfma_f32_16x16x128_f8f6f4 v[116:119], v[144:151], v[168:175], v[116:119]
	v_mfma_f32_16x16x128_f8f6f4 v[112:115], v[160:167], v[168:175], v[112:115]
	v_mfma_f32_16x16x128_f8f6f4 v[100:103], v[144:151], v[176:183], v[100:103]
	v_mfma_f32_16x16x128_f8f6f4 v[96:99], v[160:167], v[176:183], v[96:99]
	v_mfma_f32_16x16x128_f8f6f4 v[168:171], v[144:151], v[184:191], v[84:87]
	v_mfma_f32_16x16x128_f8f6f4 v[172:175], v[160:167], v[184:191], v[80:83]
	v_mfma_f32_16x16x128_f8f6f4 v[176:179], v[144:151], v[192:199], v[68:71]
	v_mfma_f32_16x16x128_f8f6f4 v[180:183], v[160:167], v[192:199], v[64:67]
	s_setprio 0
	s_barrier
	s_mov_b32 m0, s28
	s_mov_b32 s6, s10
	s_mov_b32 s7, s11
	s_nop 1
	ds_read_b128 v[64:67], v251 offset:16384
	ds_read_b128 v[72:75], v251 offset:18432
	ds_read_b128 v[68:71], v252 offset:16384
	ds_read_b128 v[76:79], v252 offset:18432
	ds_read_b128 v[80:83], v251 offset:20480
	ds_read_b128 v[88:91], v251 offset:22528
	ds_read_b128 v[84:87], v252 offset:20480
	ds_read_b128 v[92:95], v252 offset:22528
	buffer_load_dwordx4 v159, s[4:7], s65 offen lds
	s_mov_b32 m0, s29
	s_add_i32 s68, s65, 0x40000
	buffer_load_dwordx4 v244, s[4:7], s65 offen lds
	s_mov_b32 m0, s30
	s_nop 0
	buffer_load_dwordx4 v159, s[4:7], s68 offen lds
	s_mov_b32 m0, s33
	s_nop 0
	buffer_load_dwordx4 v244, s[4:7], s68 offen lds
	s_mov_b32 m0, s27
	s_nop 0
	buffer_load_dwordx4 v247, s[8:11], s67 offen lds
	s_mov_b32 m0, s34
	s_nop 0
	buffer_load_dwordx4 v248, s[8:11], s67 offen lds
	s_waitcnt vmcnt(8)
	s_waitcnt lgkmcnt(0)
	s_barrier
	s_setprio 1
	s_waitcnt lgkmcnt(5)
	v_mfma_f32_16x16x128_f8f6f4 v[60:63], v[128:135], v[64:71], v[60:63]
	v_mfma_f32_16x16x128_f8f6f4 v[56:59], v[136:143], v[64:71], v[56:59]
	s_waitcnt lgkmcnt(4)
	v_mfma_f32_16x16x128_f8f6f4 v[184:187], v[128:135], v[72:79], v[44:47]
	v_mfma_f32_16x16x128_f8f6f4 v[188:191], v[136:143], v[72:79], v[40:43]
	s_waitcnt lgkmcnt(1)
	v_mfma_f32_16x16x128_f8f6f4 v[192:195], v[128:135], v[80:87], v[28:31]
	v_mfma_f32_16x16x128_f8f6f4 v[196:199], v[136:143], v[80:87], v[24:27]
	s_waitcnt lgkmcnt(0)
	v_mfma_f32_16x16x128_f8f6f4 v[212:215], v[128:135], v[88:95], v[12:15]
	v_mfma_f32_16x16x128_f8f6f4 v[216:219], v[136:143], v[88:95], v[8:11]
	s_setprio 0
	s_setprio 1
	v_mfma_f32_16x16x128_f8f6f4 v[52:55], v[144:151], v[64:71], v[52:55]
	v_mfma_f32_16x16x128_f8f6f4 v[48:51], v[160:167], v[64:71], v[48:51]
	v_mfma_f32_16x16x128_f8f6f4 v[220:223], v[144:151], v[72:79], v[36:39]
	v_mfma_f32_16x16x128_f8f6f4 v[224:227], v[160:167], v[72:79], v[32:35]
	v_mfma_f32_16x16x128_f8f6f4 v[228:231], v[144:151], v[80:87], v[20:23]
	v_mfma_f32_16x16x128_f8f6f4 v[232:235], v[160:167], v[80:87], v[16:19]
	v_mfma_f32_16x16x128_f8f6f4 v[236:239], v[144:151], v[88:95], v[4:7]
	v_mfma_f32_16x16x128_f8f6f4 v[240:243], v[160:167], v[88:95], v[0:3]
	s_setprio 0
	s_barrier
	s_add_i32 s68, 0, 0x18000
	s_nop 2
	s_add_i32 s68, 0, 0x1c000
	ds_read_b128 v[0:3], v245 offset:32768
	ds_read_b128 v[16:19], v245 offset:34816
	ds_read_b128 v[4:7], v246 offset:32768
	ds_read_b128 v[20:23], v246 offset:34816
	ds_read_b128 v[128:131], v245 offset:49152
	ds_read_b128 v[136:139], v245 offset:51200
	ds_read_b128 v[132:135], v246 offset:49152
	ds_read_b128 v[140:143], v246 offset:51200
	s_mov_b32 m0, s35
	ds_read_b128 v[8:11], v251 offset:32768
	ds_read_b128 v[24:27], v251 offset:34816
	ds_read_b128 v[12:15], v252 offset:32768
	ds_read_b128 v[28:31], v252 offset:34816
	ds_read_b128 v[32:35], v251 offset:36864
	ds_read_b128 v[40:43], v251 offset:38912
	ds_read_b128 v[36:39], v252 offset:36864
	ds_read_b128 v[44:47], v252 offset:38912
	buffer_load_dwordx4 v249, s[8:11], s67 offen lds
	s_mov_b32 m0, s36
	s_nop 0
	buffer_load_dwordx4 v250, s[8:11], s67 offen lds
	s_waitcnt vmcnt(8)
	s_waitcnt lgkmcnt(0)
	s_barrier
	s_setprio 1
	s_waitcnt lgkmcnt(5)
	v_mfma_f32_16x16x128_f8f6f4 v[124:127], v[0:7], v[8:15], v[124:127]
	v_mfma_f32_16x16x128_f8f6f4 v[120:123], v[16:23], v[8:15], v[120:123]
	s_waitcnt lgkmcnt(4)
	v_mfma_f32_16x16x128_f8f6f4 v[108:111], v[0:7], v[24:31], v[108:111]
	v_mfma_f32_16x16x128_f8f6f4 v[104:107], v[16:23], v[24:31], v[104:107]
	s_waitcnt lgkmcnt(1)
	v_mfma_f32_16x16x128_f8f6f4 v[92:95], v[0:7], v[32:39], v[152:155]
	v_mfma_f32_16x16x128_f8f6f4 v[88:91], v[16:23], v[32:39], v[200:203]
	s_waitcnt lgkmcnt(0)
	v_mfma_f32_16x16x128_f8f6f4 v[76:79], v[0:7], v[40:47], v[204:207]
	v_mfma_f32_16x16x128_f8f6f4 v[72:75], v[16:23], v[40:47], v[208:211]
	s_setprio 0
	s_setprio 1
	v_mfma_f32_16x16x128_f8f6f4 v[116:119], v[128:135], v[8:15], v[116:119]
	v_mfma_f32_16x16x128_f8f6f4 v[112:115], v[136:143], v[8:15], v[112:115]
	v_mfma_f32_16x16x128_f8f6f4 v[100:103], v[128:135], v[24:31], v[100:103]
	v_mfma_f32_16x16x128_f8f6f4 v[96:99], v[136:143], v[24:31], v[96:99]
	v_mfma_f32_16x16x128_f8f6f4 v[84:87], v[128:135], v[32:39], v[168:171]
	v_mfma_f32_16x16x128_f8f6f4 v[80:83], v[136:143], v[32:39], v[172:175]
	v_mfma_f32_16x16x128_f8f6f4 v[68:71], v[128:135], v[40:47], v[176:179]
	v_mfma_f32_16x16x128_f8f6f4 v[64:67], v[136:143], v[40:47], v[180:183]
	s_setprio 0
	s_barrier
	s_mov_b32 m0, s38
	s_add_i32 s67, s65, 0x80
	ds_read_b128 v[32:35], v251 offset:49152
	ds_read_b128 v[144:147], v251 offset:51200
	ds_read_b128 v[36:39], v252 offset:49152
	ds_read_b128 v[148:151], v252 offset:51200
	ds_read_b128 v[160:163], v251 offset:53248
	ds_read_b128 v[168:171], v251 offset:55296
	ds_read_b128 v[164:167], v252 offset:53248
	ds_read_b128 v[172:175], v252 offset:55296
	buffer_load_dwordx4 v159, s[4:7], s67 offen lds
	s_mov_b32 m0, s39
	s_add_i32 s65, s65, 0x40080
	buffer_load_dwordx4 v244, s[4:7], s67 offen lds
	s_mov_b32 m0, s42
	s_nop 0
	buffer_load_dwordx4 v159, s[4:7], s65 offen lds
	s_mov_b32 m0, s43
	s_nop 0
	buffer_load_dwordx4 v244, s[4:7], s65 offen lds
	s_mov_b32 m0, s40
	s_nop 0
	buffer_load_dwordx4 v247, s[8:11], s66 offen lds
	s_mov_b32 m0, s41
	s_nop 0
	buffer_load_dwordx4 v248, s[8:11], s66 offen lds
	s_waitcnt vmcnt(8)
	s_waitcnt lgkmcnt(0)
	s_barrier
	s_setprio 1
	s_waitcnt lgkmcnt(5)
	v_mfma_f32_16x16x128_f8f6f4 v[60:63], v[0:7], v[32:39], v[60:63]
	v_mfma_f32_16x16x128_f8f6f4 v[56:59], v[16:23], v[32:39], v[56:59]
	s_waitcnt lgkmcnt(4)
	v_mfma_f32_16x16x128_f8f6f4 v[44:47], v[0:7], v[144:151], v[184:187]
	v_mfma_f32_16x16x128_f8f6f4 v[40:43], v[16:23], v[144:151], v[188:191]
	s_waitcnt lgkmcnt(1)
	v_mfma_f32_16x16x128_f8f6f4 v[28:31], v[0:7], v[160:167], v[192:195]
	v_mfma_f32_16x16x128_f8f6f4 v[24:27], v[16:23], v[160:167], v[196:199]
	s_waitcnt lgkmcnt(0)
	v_mfma_f32_16x16x128_f8f6f4 v[12:15], v[0:7], v[168:175], v[212:215]
	v_mfma_f32_16x16x128_f8f6f4 v[8:11], v[16:23], v[168:175], v[216:219]
	s_setprio 0
	s_setprio 1
	v_mfma_f32_16x16x128_f8f6f4 v[52:55], v[128:135], v[32:39], v[52:55]
	v_mfma_f32_16x16x128_f8f6f4 v[48:51], v[136:143], v[32:39], v[48:51]
	v_mfma_f32_16x16x128_f8f6f4 v[36:39], v[128:135], v[144:151], v[220:223]
	v_mfma_f32_16x16x128_f8f6f4 v[32:35], v[136:143], v[144:151], v[224:227]
	v_mfma_f32_16x16x128_f8f6f4 v[20:23], v[128:135], v[160:167], v[228:231]
	v_mfma_f32_16x16x128_f8f6f4 v[16:19], v[136:143], v[160:167], v[232:235]
	v_mfma_f32_16x16x128_f8f6f4 v[4:7], v[128:135], v[168:175], v[236:239]
	v_mfma_f32_16x16x128_f8f6f4 v[0:3], v[136:143], v[168:175], v[240:243]
	s_setprio 0
	s_add_i32 s63, s63, 2
	s_addk_i32 s64, 0x100
	s_cmp_gt_u32 s63, 13
	s_barrier
	s_cbranch_scc1 .LBB0_2201
	s_cmpk_lg_i32 s64, 0x780
	s_cbranch_scc1 .Lp6_join

.Lp7_fast:
.Lp7_join:
	ds_read_b128 v[128:131], v244 offset:0
	ds_read_b128 v[138:141], v244 offset:2048
	ds_read_b128 v[132:135], v245 offset:0
	ds_read_b128 v[142:145], v245 offset:2048
	ds_read_b128 v[146:149], v244 offset:16384
	ds_read_b128 v[154:157], v244 offset:18432
	ds_read_b128 v[150:153], v245 offset:16384
	ds_read_b128 v[158:161], v245 offset:18432
	s_add_i32 s6, s61, 0xffffff80
	s_add_i32 s7, s6, s56
	s_cmpk_eq_i32 s61, 0x880
	s_cselect_b32 s64, s35, s53
	s_cselect_b32 s6, 0, s6
	s_cselect_b32 s63, 0x80, s61
	s_cselect_b32 s62, s29, s7
	s_add_i32 s7, s53, s61
	s_add_i32 s63, s64, s63
	s_addk_i32 s7, 0xff00
	s_add_i32 s64, s64, s6
	s_mov_b32 m0, s44
	ds_read_b128 v[162:165], v250
	ds_read_b128 v[170:173], v250 offset:2048
	ds_read_b128 v[166:169], v251
	ds_read_b128 v[174:177], v251 offset:2048
	ds_read_b128 v[178:181], v250 offset:4096
	ds_read_b128 v[186:189], v250 offset:6144
	ds_read_b128 v[182:185], v251 offset:4096
	ds_read_b128 v[190:193], v251 offset:6144
	buffer_load_dwordx4 v248, s[8:11], s7 offen lds
	s_mov_b32 m0, s47
	s_nop 0
	buffer_load_dwordx4 v249, s[8:11], s7 offen lds
	s_waitcnt vmcnt(8)
	s_waitcnt lgkmcnt(0)
	s_barrier
	s_setprio 1
	s_waitcnt lgkmcnt(0)
	v_mfma_f32_16x16x128_f8f6f4 v[124:127], v[128:135], v[162:169], v[124:127]
	v_mfma_f32_16x16x128_f8f6f4 v[120:123], v[138:145], v[162:169], v[120:123]
	v_mfma_f32_16x16x128_f8f6f4 v[116:119], v[128:135], v[170:177], v[116:119]
	v_mfma_f32_16x16x128_f8f6f4 v[112:115], v[138:145], v[170:177], v[112:115]
	v_mfma_f32_16x16x128_f8f6f4 v[194:197], v[128:135], v[178:185], v[92:95]
	v_mfma_f32_16x16x128_f8f6f4 v[198:201], v[138:145], v[178:185], v[88:91]
	v_mfma_f32_16x16x128_f8f6f4 v[202:205], v[128:135], v[186:193], v[84:87]
	v_mfma_f32_16x16x128_f8f6f4 v[206:209], v[138:145], v[186:193], v[80:83]
	s_setprio 0
	s_setprio 1
	v_mfma_f32_16x16x128_f8f6f4 v[108:111], v[146:153], v[162:169], v[108:111]
	v_mfma_f32_16x16x128_f8f6f4 v[104:107], v[154:161], v[162:169], v[104:107]
	v_mfma_f32_16x16x128_f8f6f4 v[100:103], v[146:153], v[170:177], v[100:103]
	v_mfma_f32_16x16x128_f8f6f4 v[96:99], v[154:161], v[170:177], v[96:99]
	v_mfma_f32_16x16x128_f8f6f4 v[162:165], v[146:153], v[178:185], v[76:79]
	v_mfma_f32_16x16x128_f8f6f4 v[166:169], v[154:161], v[178:185], v[72:75]
	v_mfma_f32_16x16x128_f8f6f4 v[170:173], v[146:153], v[186:193], v[68:71]
	v_mfma_f32_16x16x128_f8f6f4 v[174:177], v[154:161], v[186:193], v[64:67]
	s_setprio 0
	s_barrier
	s_mov_b32 m0, s26
	s_mov_b32 s6, s10
	s_mov_b32 s7, s11
	s_nop 1
	ds_read_b128 v[64:67], v250 offset:16384
	ds_read_b128 v[72:75], v250 offset:18432
	ds_read_b128 v[68:71], v251 offset:16384
	ds_read_b128 v[76:79], v251 offset:18432
	ds_read_b128 v[80:83], v250 offset:20480
	ds_read_b128 v[88:91], v250 offset:22528
	ds_read_b128 v[84:87], v251 offset:20480
	ds_read_b128 v[92:95], v251 offset:22528
	buffer_load_dwordx4 v242, s[4:7], s62 offen lds
	s_mov_b32 m0, s27
	s_add_i32 s65, s62, 0x40000
	buffer_load_dwordx4 v243, s[4:7], s62 offen lds
	s_mov_b32 m0, s28
	s_nop 0
	buffer_load_dwordx4 v242, s[4:7], s65 offen lds
	s_mov_b32 m0, s30
	s_nop 0
	buffer_load_dwordx4 v243, s[4:7], s65 offen lds
	s_mov_b32 m0, s25
	s_nop 0
	buffer_load_dwordx4 v246, s[8:11], s64 offen lds
	s_mov_b32 m0, s31
	s_nop 0
	buffer_load_dwordx4 v247, s[8:11], s64 offen lds
	s_waitcnt vmcnt(8)
	s_waitcnt lgkmcnt(0)
	s_barrier
	s_setprio 1
	s_waitcnt lgkmcnt(5)
	v_mfma_f32_16x16x128_f8f6f4 v[60:63], v[128:135], v[64:71], v[60:63]
	v_mfma_f32_16x16x128_f8f6f4 v[56:59], v[138:145], v[64:71], v[56:59]
	s_waitcnt lgkmcnt(4)
	v_mfma_f32_16x16x128_f8f6f4 v[52:55], v[128:135], v[72:79], v[52:55]
	v_mfma_f32_16x16x128_f8f6f4 v[48:51], v[138:145], v[72:79], v[48:51]
	s_waitcnt lgkmcnt(1)
	v_mfma_f32_16x16x128_f8f6f4 v[178:181], v[128:135], v[80:87], v[28:31]
	v_mfma_f32_16x16x128_f8f6f4 v[182:185], v[138:145], v[80:87], v[24:27]
	s_waitcnt lgkmcnt(0)
	v_mfma_f32_16x16x128_f8f6f4 v[186:189], v[128:135], v[88:95], v[20:23]
	v_mfma_f32_16x16x128_f8f6f4 v[190:193], v[138:145], v[88:95], v[16:19]
	s_setprio 0
	s_setprio 1
	v_mfma_f32_16x16x128_f8f6f4 v[210:213], v[146:153], v[64:71], v[44:47]
	v_mfma_f32_16x16x128_f8f6f4 v[214:217], v[154:161], v[64:71], v[40:43]
	v_mfma_f32_16x16x128_f8f6f4 v[218:221], v[146:153], v[72:79], v[36:39]
	v_mfma_f32_16x16x128_f8f6f4 v[222:225], v[154:161], v[72:79], v[32:35]
	v_mfma_f32_16x16x128_f8f6f4 v[226:229], v[146:153], v[80:87], v[12:15]
	v_mfma_f32_16x16x128_f8f6f4 v[230:233], v[154:161], v[80:87], v[8:11]
	v_mfma_f32_16x16x128_f8f6f4 v[234:237], v[146:153], v[88:95], v[4:7]
	v_mfma_f32_16x16x128_f8f6f4 v[238:241], v[154:161], v[88:95], v[0:3]
	s_setprio 0
	s_barrier
	s_add_i32 s65, 0, 0x18000
	s_nop 2
	s_add_i32 s65, 0, 0x1c000
	ds_read_b128 v[0:3], v244 offset:32768
	ds_read_b128 v[8:11], v244 offset:34816
	ds_read_b128 v[4:7], v245 offset:32768
	ds_read_b128 v[12:15], v245 offset:34816
	ds_read_b128 v[128:131], v244 offset:49152
	ds_read_b128 v[138:141], v244 offset:51200
	ds_read_b128 v[132:135], v245 offset:49152
	ds_read_b128 v[142:145], v245 offset:51200
	s_mov_b32 m0, s33
	ds_read_b128 v[16:19], v250 offset:32768
	ds_read_b128 v[24:27], v250 offset:34816
	ds_read_b128 v[20:23], v251 offset:32768
	ds_read_b128 v[28:31], v251 offset:34816
	ds_read_b128 v[32:35], v250 offset:36864
	ds_read_b128 v[40:43], v250 offset:38912
	ds_read_b128 v[36:39], v251 offset:36864
	ds_read_b128 v[44:47], v251 offset:38912
	buffer_load_dwordx4 v248, s[8:11], s64 offen lds
	s_mov_b32 m0, s34
	s_nop 0
	buffer_load_dwordx4 v249, s[8:11], s64 offen lds
	s_waitcnt vmcnt(8)
	s_waitcnt lgkmcnt(0)
	s_barrier
	s_setprio 1
	s_waitcnt lgkmcnt(5)
	v_mfma_f32_16x16x128_f8f6f4 v[124:127], v[0:7], v[16:23], v[124:127]
	v_mfma_f32_16x16x128_f8f6f4 v[120:123], v[8:15], v[16:23], v[120:123]
	s_waitcnt lgkmcnt(4)
	v_mfma_f32_16x16x128_f8f6f4 v[116:119], v[0:7], v[24:31], v[116:119]
	v_mfma_f32_16x16x128_f8f6f4 v[112:115], v[8:15], v[24:31], v[112:115]
	s_waitcnt lgkmcnt(1)
	v_mfma_f32_16x16x128_f8f6f4 v[92:95], v[0:7], v[32:39], v[194:197]
	v_mfma_f32_16x16x128_f8f6f4 v[88:91], v[8:15], v[32:39], v[198:201]
	s_waitcnt lgkmcnt(0)
	v_mfma_f32_16x16x128_f8f6f4 v[84:87], v[0:7], v[40:47], v[202:205]
	v_mfma_f32_16x16x128_f8f6f4 v[80:83], v[8:15], v[40:47], v[206:209]
	s_setprio 0
	s_setprio 1
	v_mfma_f32_16x16x128_f8f6f4 v[108:111], v[128:135], v[16:23], v[108:111]
	v_mfma_f32_16x16x128_f8f6f4 v[104:107], v[138:145], v[16:23], v[104:107]
	v_mfma_f32_16x16x128_f8f6f4 v[100:103], v[128:135], v[24:31], v[100:103]
	v_mfma_f32_16x16x128_f8f6f4 v[96:99], v[138:145], v[24:31], v[96:99]
	v_mfma_f32_16x16x128_f8f6f4 v[76:79], v[128:135], v[32:39], v[162:165]
	v_mfma_f32_16x16x128_f8f6f4 v[72:75], v[138:145], v[32:39], v[166:169]
	v_mfma_f32_16x16x128_f8f6f4 v[68:71], v[128:135], v[40:47], v[170:173]
	v_mfma_f32_16x16x128_f8f6f4 v[64:67], v[138:145], v[40:47], v[174:177]
	s_setprio 0
	s_barrier
	s_mov_b32 m0, s36
	s_add_i32 s64, s62, 0x80
	ds_read_b128 v[32:35], v250 offset:49152
	ds_read_b128 v[146:149], v250 offset:51200
	ds_read_b128 v[36:39], v251 offset:49152
	ds_read_b128 v[150:153], v251 offset:51200
	ds_read_b128 v[154:157], v250 offset:53248
	ds_read_b128 v[162:165], v250 offset:55296
	ds_read_b128 v[158:161], v251 offset:53248
	ds_read_b128 v[166:169], v251 offset:55296
	buffer_load_dwordx4 v242, s[4:7], s64 offen lds
	s_mov_b32 m0, s37
	s_add_i32 s62, s62, 0x40080
	buffer_load_dwordx4 v243, s[4:7], s64 offen lds
	s_mov_b32 m0, s40
	s_nop 0
	buffer_load_dwordx4 v242, s[4:7], s62 offen lds
	s_mov_b32 m0, s41
	s_nop 0
	buffer_load_dwordx4 v243, s[4:7], s62 offen lds
	s_mov_b32 m0, s38
	s_nop 0
	buffer_load_dwordx4 v246, s[8:11], s63 offen lds
	s_mov_b32 m0, s39
	s_nop 0
	buffer_load_dwordx4 v247, s[8:11], s63 offen lds
	s_waitcnt vmcnt(8)
	s_waitcnt lgkmcnt(0)
	s_barrier
	s_setprio 1
	s_waitcnt lgkmcnt(5)
	v_mfma_f32_16x16x128_f8f6f4 v[60:63], v[0:7], v[32:39], v[60:63]
	v_mfma_f32_16x16x128_f8f6f4 v[56:59], v[8:15], v[32:39], v[56:59]
	s_waitcnt lgkmcnt(4)
	v_mfma_f32_16x16x128_f8f6f4 v[52:55], v[0:7], v[146:153], v[52:55]
	v_mfma_f32_16x16x128_f8f6f4 v[48:51], v[8:15], v[146:153], v[48:51]
	s_waitcnt lgkmcnt(1)
	v_mfma_f32_16x16x128_f8f6f4 v[28:31], v[0:7], v[154:161], v[178:181]
	v_mfma_f32_16x16x128_f8f6f4 v[24:27], v[8:15], v[154:161], v[182:185]
	s_waitcnt lgkmcnt(0)
	v_mfma_f32_16x16x128_f8f6f4 v[20:23], v[0:7], v[162:169], v[186:189]
	v_mfma_f32_16x16x128_f8f6f4 v[16:19], v[8:15], v[162:169], v[190:193]
	s_setprio 0
	s_setprio 1
	v_mfma_f32_16x16x128_f8f6f4 v[44:47], v[128:135], v[32:39], v[210:213]
	v_mfma_f32_16x16x128_f8f6f4 v[40:43], v[138:145], v[32:39], v[214:217]
	v_mfma_f32_16x16x128_f8f6f4 v[36:39], v[128:135], v[146:153], v[218:221]
	v_mfma_f32_16x16x128_f8f6f4 v[32:35], v[138:145], v[146:153], v[222:225]
	v_mfma_f32_16x16x128_f8f6f4 v[12:15], v[128:135], v[154:161], v[226:229]
	v_mfma_f32_16x16x128_f8f6f4 v[8:11], v[138:145], v[154:161], v[230:233]
	v_mfma_f32_16x16x128_f8f6f4 v[4:7], v[128:135], v[162:169], v[234:237]
	v_mfma_f32_16x16x128_f8f6f4 v[0:3], v[138:145], v[162:169], v[238:241]
	s_setprio 0
	s_add_i32 s60, s60, 2
	s_addk_i32 s61, 0x100
	s_cmp_gt_u32 s60, 13
	s_barrier
	s_cbranch_scc1 .LBB0_2279
	s_cmpk_lg_i32 s61, 0x780
	s_cbranch_scc1 .Lp7_join

.Lp11_fast:
.Lp11_join:
	ds_read_b128 v[128:131], v150 offset:0
	ds_read_b128 v[136:139], v150 offset:2048
	ds_read_b128 v[132:135], v152 offset:0
	ds_read_b128 v[140:143], v152 offset:2048
	ds_read_b128 v[154:157], v150 offset:16384
	ds_read_b128 v[162:165], v150 offset:18432
	ds_read_b128 v[158:161], v152 offset:16384
	ds_read_b128 v[166:169], v152 offset:18432
	s_add_i32 s6, s80, 0xffffff80
	s_add_i32 s7, s6, s75
	s_cmpk_eq_i32 s80, 0x880
	s_cselect_b32 s81, s71, s35
	s_cselect_b32 s11, 0x80, s80
	s_cselect_b32 s10, 0, s6
	s_cselect_b32 s6, s51, s7
	s_add_i32 s7, s81, s11
	s_add_i32 s11, s35, s80
	s_addk_i32 s11, 0xff00
	s_add_i32 s81, s81, s10
	s_mov_b32 m0, s60
	ds_read_b128 v[170:173], v148
	ds_read_b128 v[178:181], v148 offset:2048
	ds_read_b128 v[174:177], v146
	ds_read_b128 v[182:185], v146 offset:2048
	ds_read_b128 v[186:189], v148 offset:4096
	ds_read_b128 v[194:197], v148 offset:6144
	ds_read_b128 v[190:193], v146 offset:4096
	ds_read_b128 v[198:201], v146 offset:6144
	buffer_load_dwordx4 v252, s[88:91], s11 offen lds
	s_mov_b32 m0, s63
	s_nop 0
	buffer_load_dwordx4 v253, s[88:91], s11 offen lds
	s_waitcnt vmcnt(8)
	s_waitcnt lgkmcnt(0)
	s_barrier
	s_setprio 1
	s_waitcnt lgkmcnt(0)
	v_mfma_f32_16x16x128_f8f6f4 v[124:127], v[128:135], v[170:177], v[124:127]
	v_mfma_f32_16x16x128_f8f6f4 v[120:123], v[136:143], v[170:177], v[120:123]
	v_mfma_f32_16x16x128_f8f6f4 v[116:119], v[128:135], v[178:185], v[116:119]
	v_mfma_f32_16x16x128_f8f6f4 v[112:115], v[136:143], v[178:185], v[112:115]
	v_mfma_f32_16x16x128_f8f6f4 v[96:99], v[128:135], v[186:193], v[96:99]
	v_mfma_f32_16x16x128_f8f6f4 v[202:205], v[136:143], v[186:193], v[88:91]
	v_mfma_f32_16x16x128_f8f6f4 v[206:209], v[128:135], v[194:201], v[80:83]
	v_mfma_f32_16x16x128_f8f6f4 v[210:213], v[136:143], v[194:201], v[72:75]
	s_setprio 0
	s_setprio 1
	v_mfma_f32_16x16x128_f8f6f4 v[108:111], v[154:161], v[170:177], v[108:111]
	v_mfma_f32_16x16x128_f8f6f4 v[104:107], v[162:169], v[170:177], v[104:107]
	v_mfma_f32_16x16x128_f8f6f4 v[100:103], v[154:161], v[178:185], v[100:103]
	v_mfma_f32_16x16x128_f8f6f4 v[170:173], v[162:169], v[178:185], v[92:95]
	v_mfma_f32_16x16x128_f8f6f4 v[174:177], v[154:161], v[186:193], v[84:87]
	v_mfma_f32_16x16x128_f8f6f4 v[178:181], v[162:169], v[186:193], v[76:79]
	v_mfma_f32_16x16x128_f8f6f4 v[182:185], v[154:161], v[194:201], v[68:71]
	v_mfma_f32_16x16x128_f8f6f4 v[186:189], v[162:169], v[194:201], v[64:67]
	s_setprio 0
	s_barrier
	s_mov_b32 m0, s43
	s_mov_b32 s10, s90
	s_mov_b32 s11, s91
	s_nop 1
	ds_read_b128 v[64:67], v148 offset:16384
	ds_read_b128 v[72:75], v148 offset:18432
	ds_read_b128 v[68:71], v146 offset:16384
	ds_read_b128 v[76:79], v146 offset:18432
	ds_read_b128 v[80:83], v148 offset:20480
	ds_read_b128 v[88:91], v148 offset:22528
	ds_read_b128 v[84:87], v146 offset:20480
	ds_read_b128 v[92:95], v146 offset:22528
	buffer_load_dwordx4 v144, s[8:11], s6 offen lds
	s_mov_b32 m0, s44
	s_add_i32 s82, s6, 0x40000
	buffer_load_dwordx4 v145, s[8:11], s6 offen lds
	s_mov_b32 m0, s45
	s_nop 0
	buffer_load_dwordx4 v144, s[8:11], s82 offen lds
	s_mov_b32 m0, s46
	s_nop 0
	buffer_load_dwordx4 v145, s[8:11], s82 offen lds
	s_mov_b32 m0, s42
	s_nop 0
	buffer_load_dwordx4 v250, s[88:91], s81 offen lds
	s_mov_b32 m0, s47
	s_nop 0
	buffer_load_dwordx4 v251, s[88:91], s81 offen lds
	s_waitcnt vmcnt(8)
	s_waitcnt lgkmcnt(0)
	s_barrier
	s_setprio 1
	s_waitcnt lgkmcnt(5)
	v_mfma_f32_16x16x128_f8f6f4 v[60:63], v[128:135], v[64:71], v[60:63]
	v_mfma_f32_16x16x128_f8f6f4 v[56:59], v[136:143], v[64:71], v[56:59]
	s_waitcnt lgkmcnt(4)
	v_mfma_f32_16x16x128_f8f6f4 v[48:51], v[128:135], v[72:79], v[48:51]
	v_mfma_f32_16x16x128_f8f6f4 v[190:193], v[136:143], v[72:79], v[40:43]
	s_waitcnt lgkmcnt(1)
	v_mfma_f32_16x16x128_f8f6f4 v[194:197], v[128:135], v[80:87], v[32:35]
	v_mfma_f32_16x16x128_f8f6f4 v[198:201], v[136:143], v[80:87], v[24:27]
	s_waitcnt lgkmcnt(0)
	v_mfma_f32_16x16x128_f8f6f4 v[214:217], v[128:135], v[88:95], v[16:19]
	v_mfma_f32_16x16x128_f8f6f4 v[218:221], v[136:143], v[88:95], v[8:11]
	s_setprio 0
	s_setprio 1
	v_mfma_f32_16x16x128_f8f6f4 v[52:55], v[154:161], v[64:71], v[52:55]
	v_mfma_f32_16x16x128_f8f6f4 v[222:225], v[162:169], v[64:71], v[44:47]
	v_mfma_f32_16x16x128_f8f6f4 v[226:229], v[154:161], v[72:79], v[36:39]
	v_mfma_f32_16x16x128_f8f6f4 v[230:233], v[162:169], v[72:79], v[28:31]
	v_mfma_f32_16x16x128_f8f6f4 v[234:237], v[154:161], v[80:87], v[20:23]
	v_mfma_f32_16x16x128_f8f6f4 v[238:241], v[162:169], v[80:87], v[12:15]
	v_mfma_f32_16x16x128_f8f6f4 v[242:245], v[154:161], v[88:95], v[4:7]
	v_mfma_f32_16x16x128_f8f6f4 v[246:249], v[162:169], v[88:95], v[0:3]
	s_setprio 0
	s_barrier
	s_add_i32 s82, 0, 0x18000
	s_nop 2
	s_add_i32 s82, 0, 0x1c000
	ds_read_b128 v[0:3], v150 offset:32768
	ds_read_b128 v[8:11], v150 offset:34816
	ds_read_b128 v[4:7], v152 offset:32768
	ds_read_b128 v[12:15], v152 offset:34816
	ds_read_b128 v[128:131], v150 offset:49152
	ds_read_b128 v[136:139], v150 offset:51200
	ds_read_b128 v[132:135], v152 offset:49152
	ds_read_b128 v[140:143], v152 offset:51200
	s_mov_b32 m0, s48
	ds_read_b128 v[16:19], v148 offset:32768
	ds_read_b128 v[24:27], v148 offset:34816
	ds_read_b128 v[20:23], v146 offset:32768
	ds_read_b128 v[28:31], v146 offset:34816
	ds_read_b128 v[32:35], v148 offset:36864
	ds_read_b128 v[40:43], v148 offset:38912
	ds_read_b128 v[36:39], v146 offset:36864
	ds_read_b128 v[44:47], v146 offset:38912
	buffer_load_dwordx4 v252, s[88:91], s81 offen lds
	s_mov_b32 m0, s49
	s_nop 0
	buffer_load_dwordx4 v253, s[88:91], s81 offen lds
	s_waitcnt vmcnt(8)
	s_waitcnt lgkmcnt(0)
	s_barrier
	s_setprio 1
	s_waitcnt lgkmcnt(5)
	v_mfma_f32_16x16x128_f8f6f4 v[124:127], v[0:7], v[16:23], v[124:127]
	v_mfma_f32_16x16x128_f8f6f4 v[120:123], v[8:15], v[16:23], v[120:123]
	s_waitcnt lgkmcnt(4)
	v_mfma_f32_16x16x128_f8f6f4 v[116:119], v[0:7], v[24:31], v[116:119]
	v_mfma_f32_16x16x128_f8f6f4 v[112:115], v[8:15], v[24:31], v[112:115]
	s_waitcnt lgkmcnt(1)
	v_mfma_f32_16x16x128_f8f6f4 v[96:99], v[0:7], v[32:39], v[96:99]
	v_mfma_f32_16x16x128_f8f6f4 v[88:91], v[8:15], v[32:39], v[202:205]
	s_waitcnt lgkmcnt(0)
	v_mfma_f32_16x16x128_f8f6f4 v[80:83], v[0:7], v[40:47], v[206:209]
	v_mfma_f32_16x16x128_f8f6f4 v[72:75], v[8:15], v[40:47], v[210:213]
	s_setprio 0
	s_setprio 1
	v_mfma_f32_16x16x128_f8f6f4 v[108:111], v[128:135], v[16:23], v[108:111]
	v_mfma_f32_16x16x128_f8f6f4 v[104:107], v[136:143], v[16:23], v[104:107]
	v_mfma_f32_16x16x128_f8f6f4 v[100:103], v[128:135], v[24:31], v[100:103]
	v_mfma_f32_16x16x128_f8f6f4 v[92:95], v[136:143], v[24:31], v[170:173]
	v_mfma_f32_16x16x128_f8f6f4 v[84:87], v[128:135], v[32:39], v[174:177]
	v_mfma_f32_16x16x128_f8f6f4 v[76:79], v[136:143], v[32:39], v[178:181]
	v_mfma_f32_16x16x128_f8f6f4 v[68:71], v[128:135], v[40:47], v[182:185]
	v_mfma_f32_16x16x128_f8f6f4 v[64:67], v[136:143], v[40:47], v[186:189]
	s_setprio 0
	s_barrier
	s_mov_b32 m0, s52
	s_add_i32 s81, s6, 0x80
	ds_read_b128 v[154:157], v148 offset:49152
	ds_read_b128 v[162:165], v148 offset:51200
	ds_read_b128 v[158:161], v146 offset:49152
	ds_read_b128 v[166:169], v146 offset:51200
	ds_read_b128 v[170:173], v148 offset:53248
	ds_read_b128 v[178:181], v148 offset:55296
	ds_read_b128 v[174:177], v146 offset:53248
	ds_read_b128 v[182:185], v146 offset:55296
	buffer_load_dwordx4 v144, s[8:11], s81 offen lds
	s_mov_b32 m0, s53
	s_add_i32 s6, s6, 0x40080
	buffer_load_dwordx4 v145, s[8:11], s81 offen lds
	s_mov_b32 m0, s56
	s_nop 0
	buffer_load_dwordx4 v144, s[8:11], s6 offen lds
	s_mov_b32 m0, s57
	s_nop 0
	buffer_load_dwordx4 v145, s[8:11], s6 offen lds
	s_mov_b32 m0, s54
	s_nop 0
	buffer_load_dwordx4 v250, s[88:91], s7 offen lds
	s_mov_b32 m0, s55
	s_nop 0
	buffer_load_dwordx4 v251, s[88:91], s7 offen lds
	s_waitcnt vmcnt(8)
	s_waitcnt lgkmcnt(0)
	s_barrier
	s_setprio 1
	s_waitcnt lgkmcnt(5)
	v_mfma_f32_16x16x128_f8f6f4 v[60:63], v[0:7], v[154:161], v[60:63]
	v_mfma_f32_16x16x128_f8f6f4 v[56:59], v[8:15], v[154:161], v[56:59]
	s_waitcnt lgkmcnt(4)
	v_mfma_f32_16x16x128_f8f6f4 v[48:51], v[0:7], v[162:169], v[48:51]
	v_mfma_f32_16x16x128_f8f6f4 v[40:43], v[8:15], v[162:169], v[190:193]
	s_waitcnt lgkmcnt(1)
	v_mfma_f32_16x16x128_f8f6f4 v[32:35], v[0:7], v[170:177], v[194:197]
	v_mfma_f32_16x16x128_f8f6f4 v[24:27], v[8:15], v[170:177], v[198:201]
	s_waitcnt lgkmcnt(0)
	v_mfma_f32_16x16x128_f8f6f4 v[16:19], v[0:7], v[178:185], v[214:217]
	v_mfma_f32_16x16x128_f8f6f4 v[8:11], v[8:15], v[178:185], v[218:221]
	s_setprio 0
	s_setprio 1
	v_mfma_f32_16x16x128_f8f6f4 v[52:55], v[128:135], v[154:161], v[52:55]
	v_mfma_f32_16x16x128_f8f6f4 v[44:47], v[136:143], v[154:161], v[222:225]
	v_mfma_f32_16x16x128_f8f6f4 v[36:39], v[128:135], v[162:169], v[226:229]
	v_mfma_f32_16x16x128_f8f6f4 v[28:31], v[136:143], v[162:169], v[230:233]
	v_mfma_f32_16x16x128_f8f6f4 v[20:23], v[128:135], v[170:177], v[234:237]
	v_mfma_f32_16x16x128_f8f6f4 v[12:15], v[136:143], v[170:177], v[238:241]
	v_mfma_f32_16x16x128_f8f6f4 v[4:7], v[128:135], v[178:185], v[242:245]
	v_mfma_f32_16x16x128_f8f6f4 v[0:3], v[136:143], v[178:185], v[246:249]
	s_setprio 0
	s_add_i32 s79, s79, 2
	s_addk_i32 s80, 0x100
	s_cmp_gt_u32 s79, 13
	s_barrier
	s_cbranch_scc1 .LBB0_2574
	s_cmpk_lg_i32 s80, 0x780
	s_cbranch_scc1 .Lp11_join
